# v55 + explicit vmcnt(0) in both attention preheaders (first tile's K/V staging loads are waited for before the first LDS staging write; the per-tile ladder stays removed)
# baseline (speedup 1.0000x reference)
; DEV int ltid() { int t = threadIdx.x; asm volatile("" : "+v"(t)); return t; }
; DEV unsigned cvt_pk_bf16(float lo, float hi) { const f32x2 v = {lo, hi}; const bf16n2 r = __builtin_convertvector(v, bf16n2); return __builtin_bit_cast(unsigned, r); }
; DEV float bf2f(bf16_t v) { return __uint_as_float(((unsigned)v) << 16); }
; DEV int v_st(int k, int c) { const int kk = (k & ~0xC) | ((k & 4) << 1) | ((k & 8) >> 1); return ((kk >> 3) * 4 + (c >> 5)) * 512 + ((kk & 7) * 32 + (c & 31)) * 2; }
; DEV void fill_load(CParams& p, int wg, int slot, f32x4 (&ld)[4]) {
;   const FillDesc d = fill_decode(p, wg, slot); const int tid = ltid(), tx = tid & 15, ty = tid >> 4;
;   const float* sp = d.src + (long)(d.kh + 4 * ty) * d.ldsrc + d.n0 + 4 * tx;
; DEV void attn_unit(const bf16_t* __restrict__ Qb, const bf16_t* __restrict__ Kh, const bf16_t* __restrict__ Vh, const float* __restrict__ rp, bf16_t* __restrict__ Ob, CParams& fp, int fwg, int fbase, int fn) {
;     ...
; #pragma unroll
;     for (int dd = 0; dd < 2; ++dd) {
;       const int a0 = 16 * dd + 8 * hi;
;       const f32x4 c0 = *(const f32x4*)(rr + a0), c1 = *(const f32x4*)(rr + a0 + 4), s0 = *(const f32x4*)(rr + 32 + a0), s1 = *(const f32x4*)(rr + 32 + a0 + 4);
;       float cs[8] = {c0[0], c0[1], c0[2], c0[3], c1[0], c1[1], c1[2], c1[3]}, sn[8] = {s0[0], s0[1], s0[2], s0[3], s1[0], s1[1], s1[2], s1[3]};
;       const bf16x8 x1 = qr[8 + dd], x2 = qr[10 + dd]; bf16x8 y1, y2;
; #pragma unroll
;       for (int j = 0; j < 8; j += 2) {
;         const float a1 = bf2f((bf16_t)x1[j]), a2 = bf2f((bf16_t)x2[j]), b1 = bf2f((bf16_t)x1[j + 1]), b2 = bf2f((bf16_t)x2[j + 1]);
;         const unsigned u1 = cvt_pk_bf16(a1 * cs[j] - a2 * sn[j], b1 * cs[j + 1] - b2 * sn[j + 1]);
;         const unsigned u2 = cvt_pk_bf16(a1 * sn[j] + a2 * cs[j], b1 * sn[j + 1] + b2 * cs[j + 1]);
;         y1[j] = (short)(u1 & 0xffff); y1[j + 1] = (short)(u1 >> 16); y2[j] = (short)(u2 & 0xffff); y2[j + 1] = (short)(u2 >> 16);
;       }
;       qr[8 + dd] = y1; qr[10 + dd] = y2;
;     }
;   }
;   const int sr = tid >> 4, sc = (tid & 15) * 8, vst0 = v_st(sr, sc), vst1 = v_st(32 + sr, sc);
;   int kst[3];
; #pragma unroll
;   for (int i = 0; i < 3; ++i) { const int id = tid + 512 * i, row = id / 24, ch = id % 24; kst[i] = KSWZ2(row, ch * 16); }
.LBB0_890:
	s_waitcnt vmcnt(11)
	v_and_b32_e32 v83, 0xffff0000, v58
	v_lshlrev_b32_e32 v82, 16, v58
	s_waitcnt vmcnt(9)
	v_and_b32_e32 v85, 0xffff0000, v50
	v_lshlrev_b32_e32 v84, 16, v50
	s_waitcnt vmcnt(4)
	v_pk_mul_f32 v[86:87], v[66:67], v[84:85]
	v_pk_mul_f32 v[66:67], v[66:67], v[82:83]
	v_pk_fma_f32 v[86:87], v[62:63], v[82:83], v[86:87] neg_lo:[0,0,1] neg_hi:[0,0,1]
	v_pk_fma_f32 v[62:63], v[62:63], v[84:85], v[66:67]
	v_lshlrev_b32_e32 v58, 16, v51
	v_cvt_pk_bf16_f32 v136, v62, v63
	v_and_b32_e32 v63, 0xffff0000, v59
	v_lshlrev_b32_e32 v62, 16, v59
	v_and_b32_e32 v59, 0xffff0000, v51
	v_pk_mul_f32 v[50:51], v[68:69], v[58:59]
	s_mov_b32 s21, 0x2aaaaaab
	v_pk_fma_f32 v[50:51], v[64:65], v[62:63], v[50:51] neg_lo:[0,0,1] neg_hi:[0,0,1]
	s_lshl_b32 s19, s20, s19
	v_cvt_pk_bf16_f32 v133, v50, v51
	v_pk_mul_f32 v[50:51], v[68:69], v[62:63]
	s_and_b32 s19, s19, 0x780
	v_pk_fma_f32 v[50:51], v[64:65], v[58:59], v[50:51]
	v_and_b32_e32 v59, 0xffff0000, v52
	v_lshlrev_b32_e32 v58, 16, v52
	v_cvt_pk_bf16_f32 v137, v50, v51
	v_and_b32_e32 v51, 0xffff0000, v60
	v_lshlrev_b32_e32 v50, 16, v60
	v_pk_mul_f32 v[62:63], v[54:55], v[58:59]
	s_mov_b32 s17, 0
	v_pk_fma_f32 v[62:63], v[46:47], v[50:51], v[62:63] neg_lo:[0,0,1] neg_hi:[0,0,1]
	v_pk_mul_f32 v[50:51], v[54:55], v[50:51]
	v_mov_b32_e32 v67, 0
	v_pk_fma_f32 v[46:47], v[46:47], v[58:59], v[50:51]
	v_and_b32_e32 v51, 0xffff0000, v53
	v_lshlrev_b32_e32 v50, 16, v53
	v_cvt_pk_bf16_f32 v138, v46, v47
	v_and_b32_e32 v47, 0xffff0000, v61
	v_lshlrev_b32_e32 v46, 16, v61
	v_pk_mul_f32 v[52:53], v[56:57], v[50:51]
	v_and_b32_e32 v77, 0x3fffffc0, v1
	v_pk_fma_f32 v[52:53], v[48:49], v[46:47], v[52:53] neg_lo:[0,0,1] neg_hi:[0,0,1]
	v_pk_mul_f32 v[46:47], v[56:57], v[46:47]
	s_add_i32 s77, 0, 0x18000
	v_pk_fma_f32 v[46:47], v[48:49], v[50:51], v[46:47]
	v_and_b32_e32 v49, 0xffff0000, v22
	v_cvt_pk_bf16_f32 v139, v46, v47
	v_and_b32_e32 v47, 0xffff0000, v30
	v_lshlrev_b32_e32 v46, 16, v30
	v_lshlrev_b32_e32 v48, 16, v22
	s_waitcnt vmcnt(0)
	v_pk_mul_f32 v[50:51], v[42:43], v[48:49]
	v_pk_mul_f32 v[42:43], v[42:43], v[46:47]
	v_pk_fma_f32 v[50:51], v[38:39], v[46:47], v[50:51] neg_lo:[0,0,1] neg_hi:[0,0,1]
	v_pk_fma_f32 v[38:39], v[38:39], v[48:49], v[42:43]
	v_lshlrev_b32_e32 v30, 16, v23
	v_cvt_pk_bf16_f32 v144, v38, v39
	v_and_b32_e32 v39, 0xffff0000, v31
	v_lshlrev_b32_e32 v38, 16, v31
	v_and_b32_e32 v31, 0xffff0000, v23
	v_pk_mul_f32 v[22:23], v[44:45], v[30:31]
	v_lshl_add_u32 v185, v77, 2, s77
	v_pk_fma_f32 v[22:23], v[40:41], v[38:39], v[22:23] neg_lo:[0,0,1] neg_hi:[0,0,1]
	v_mov_b32_e32 v77, v67
	v_cvt_pk_bf16_f32 v141, v22, v23
	v_pk_mul_f32 v[22:23], v[44:45], v[38:39]
	s_movk_i32 s28, 0xc0
	v_pk_fma_f32 v[22:23], v[40:41], v[30:31], v[22:23]
	v_and_b32_e32 v31, 0xffff0000, v24
	v_lshlrev_b32_e32 v30, 16, v24
	v_cvt_pk_bf16_f32 v145, v22, v23
	v_and_b32_e32 v23, 0xffff0000, v32
	v_lshlrev_b32_e32 v22, 16, v32
	v_pk_mul_f32 v[38:39], v[34:35], v[30:31]
	v_cvt_pk_bf16_f32 v134, v62, v63
	v_pk_fma_f32 v[38:39], v[26:27], v[22:23], v[38:39] neg_lo:[0,0,1] neg_hi:[0,0,1]
	v_pk_mul_f32 v[22:23], v[34:35], v[22:23]
	v_cvt_pk_bf16_f32 v135, v52, v53
	v_pk_fma_f32 v[22:23], v[26:27], v[30:31], v[22:23]
	v_and_b32_e32 v27, 0xffff0000, v25
	v_lshlrev_b32_e32 v26, 16, v25
	v_cvt_pk_bf16_f32 v146, v22, v23
	v_and_b32_e32 v23, 0xffff0000, v33
	v_lshlrev_b32_e32 v22, 16, v33
	v_pk_mul_f32 v[24:25], v[36:37], v[26:27]
	v_cvt_pk_bf16_f32 v140, v50, v51
	v_pk_fma_f32 v[24:25], v[28:29], v[22:23], v[24:25] neg_lo:[0,0,1] neg_hi:[0,0,1]
	v_pk_mul_f32 v[22:23], v[36:37], v[22:23]
	v_cvt_pk_bf16_f32 v143, v24, v25
	v_pk_fma_f32 v[22:23], v[28:29], v[26:27], v[22:23]
	v_and_b32_e32 v25, 3, v74
	v_cvt_pk_bf16_f32 v147, v22, v23
	v_and_b32_e32 v22, 0xfffff0, v74
	v_lshlrev_b32_e32 v23, 1, v74
	v_and_or_b32 v22, v23, 8, v22
	v_lshrrev_b32_e32 v23, 1, v74
	v_and_or_b32 v23, v23, 4, v25
	v_and_b32_e32 v25, 0xfffff0, v78
	v_lshlrev_b32_e32 v26, 1, v78
	v_and_or_b32 v25, v26, 8, v25
	v_lshrrev_b32_e32 v22, 1, v22
	v_lshrrev_b32_e32 v24, 5, v80
	v_lshrrev_b32_e32 v25, 1, v25
	v_or_b32_e32 v22, v22, v24
	v_or_b32_e32 v24, v25, v24
	v_mul_hi_i32 v25, v1, s21
	v_lshrrev_b32_e32 v26, 31, v25
	v_ashrrev_i32_e32 v25, 2, v25
	v_add_u32_e32 v25, v25, v26
	v_mul_lo_u32 v26, v25, 24
	v_sub_u32_e32 v26, v1, v26
	v_lshlrev_b32_e32 v27, 9, v25
	v_bitop3_b32 v25, v25, v26, 15 bitop3:0x6c
	v_lshl_add_u32 v195, v25, 4, v27
	v_add_u32_e32 v25, 0x200, v1
	v_mul_hi_i32 v26, v25, s21
	v_lshrrev_b32_e32 v27, 31, v26
	v_ashrrev_i32_e32 v26, 2, v26
	v_add_u32_e32 v26, v26, v27
	v_mul_lo_u32 v27, v26, 24
	v_sub_u32_e32 v25, v25, v27
	v_lshlrev_b32_e32 v27, 9, v26
	v_bitop3_b32 v25, v26, v25, 15 bitop3:0x6c
	v_lshl_add_u32 v196, v25, 4, v27
	v_add_u32_e32 v25, 0x400, v1
	v_mul_hi_i32 v26, v25, s21
	v_lshrrev_b32_e32 v27, 31, v26
	v_ashrrev_i32_e32 v26, 2, v26
	v_add_u32_e32 v26, v26, v27
	v_mul_lo_u32 v27, v26, 24
	v_sub_u32_e32 v25, v25, v27
	v_lshlrev_b32_e32 v27, 9, v26
	v_bitop3_b32 v25, v26, v25, 15 bitop3:0x6c
	v_lshlrev_b32_e32 v22, 9, v22
	v_lshlrev_b32_e32 v23, 6, v23
	v_lshl_add_u32 v197, v25, 4, v27
	v_and_b32_e32 v25, 48, v76
	v_lshlrev_b32_e32 v24, 9, v24
	v_or3_b32 v198, v22, v23, v25
	v_lshlrev_b32_e32 v22, 4, v187
	v_or3_b32 v199, v24, v23, v25
	v_and_b32_e32 v27, 0xc0, v22
	v_lshlrev_b32_e32 v22, 1, v187
	v_mov_b32_e32 v24, v0
	v_and_b32_e32 v28, 32, v22
	s_lshl_b32 s21, s2, 6
	s_and_b32 s53, s21, 64
	v_ashrrev_i32_e32 v22, 2, v24
	s_lshl_b32 s21, s20, 7
	v_and_b32_e32 v22, -4, v22
	s_and_b32 s16, s16, s21
	v_add_u32_e32 v22, s19, v22
	s_or_b32 s16, s16, s53
	v_mad_i64_i32 v[22:23], s[20:21], s18, v22, 0
; DEV int ltid() { int t = threadIdx.x; asm volatile("" : "+v"(t)); return t; }
; DEV int v_rd_base(int lane) { return ((lane & 3) << 3) | (((lane >> 2) & 3) << 6) | (((lane >> 4) & 1) << 5) | (((lane >> 5) & 1) << 8); }
; #define SLOAD(k0) do { vs0 = *reinterpret_cast<const bf16x8*>(Vh + (long)((k0) + sr) * DV + sc); vs1 = *reinterpret_cast<const bf16x8*>(Vh + (long)((k0) + 32 + sr) * DV + sc); \
;     const bf16_t* kp_ = Kh + (long)(k0) * QK + tid * 8; ks0 = *reinterpret_cast<const bf16x8*>(kp_); ks1 = *reinterpret_cast<const bf16x8*>(kp_ + 4096); ks2 = *reinterpret_cast<const bf16x8*>(kp_ + 8192); } while (0)
; #define SWRITE(b) do { *(bf16x8*)(V_lds + (b) * SHM_V + vst0) = vs0; *(bf16x8*)(V_lds + (b) * SHM_V + vst1) = vs1; \
;     *(bf16x8*)(K_lds + (b) * SHM_K + kst[0]) = ks0; *(bf16x8*)(K_lds + (b) * SHM_K + kst[1]) = ks1; *(bf16x8*)(K_lds + (b) * SHM_K + kst[2]) = ks2; } while (0)
; #define SWAIT() asm volatile("s_waitcnt vmcnt(0)" ::: "memory")
; DEV void fill_load(CParams& p, int wg, int slot, f32x4 (&ld)[4]) {
;   const FillDesc d = fill_decode(p, wg, slot); const int tid = ltid(), tx = tid & 15, ty = tid >> 4;
;   const float* sp = d.src + (long)(d.kh + 4 * ty) * d.ldsrc + d.n0 + 4 * tx;
; #pragma unroll
;   for (int r = 0; r < 4; ++r) ld[r] = *(const f32x4*)(sp + (long)r * d.ldsrc);
; DEV void attn_unit(const bf16_t* __restrict__ Qb, const bf16_t* __restrict__ Kh, const bf16_t* __restrict__ Vh, const float* __restrict__ rp, bf16_t* __restrict__ Ob, CParams& fp, int fwg, int fbase, int fn) {
;     ...
;   const int vb0 = (int)(uintptr_t)V_lds + v_rd_base(lane);
;     ...
;   f32x16 p0, p1; float mn, al; bf16x8 pa0, pa1, pa2, pa3; constexpr int NTL = KEYS / KVBLK;
;   f32x4 fld[4];
;   if (fn > 0) fill_load(fp, fwg, fbase, fld);
;   SWRITE(0); SLOAD(KVBLK); __syncthreads();
; #pragma unroll 1
;   for (int j = 0; j < NTL; ++j) {
;     const int cb = j & 1;
;     if (j + 1 < NTL) { if (j >= 2 && j < fn) asm volatile("s_waitcnt vmcnt(5)" ::: "memory"); else SWAIT(); SWRITE(cb ^ 1); }
	v_lshl_add_u64 v[22:23], v[22:23], 2, s[14:15]
	s_lshl_b32 s16, s16, 2
	v_lshlrev_b32_e32 v24, 4, v24
	v_lshl_add_u64 v[22:23], v[22:23], 0, s[16:17]
	v_and_b32_e32 v66, 0xf0, v24
	v_lshl_add_u64 v[22:23], v[22:23], 0, v[66:67]
	s_lshl_b32 s16, s18, 2
	v_lshl_add_u64 v[24:25], v[22:23], 0, s[16:17]
	global_load_dwordx4 v[168:171], v[22:23], off
	global_load_dwordx4 v[172:175], v[24:25], off
	v_lshl_add_u64 v[22:23], v[24:25], 0, s[16:17]
	v_lshl_add_u64 v[24:25], v[22:23], 0, s[16:17]
	global_load_dwordx4 v[176:179], v[22:23], off
	global_load_dwordx4 v[180:183], v[24:25], off
	v_add_u32_e32 v22, 0, v198
	ds_write_b128 v22, v[6:9]
	v_add_u32_e32 v6, 0, v199
	ds_write_b128 v6, v[2:5]
	v_add_u32_e32 v2, 0, v195
	ds_write_b128 v2, v[10:13] offset:32768
	v_add_u32_e32 v2, 0, v196
	ds_write_b128 v2, v[14:17] offset:32768
	v_add_u32_e32 v2, 0, v197
	ds_write_b128 v2, v[18:21] offset:32768
	v_lshlrev_b64 v[2:3], 8, v[74:75]
	v_lshl_add_u64 v[2:3], s[12:13], 0, v[2:3]
	v_lshl_add_u64 v[2:3], v[2:3], 0, v[76:77]
	s_movk_i32 s12, 0x4000
	v_add_co_u32_e32 v4, vcc, s12, v2
	s_movk_i32 s12, 0x6000
	s_nop 0
	v_addc_co_u32_e32 v5, vcc, 0, v3, vcc
	v_add_co_u32_e32 v2, vcc, s12, v2
	v_lshlrev_b32_e32 v26, 3, v187
	s_nop 0
	v_addc_co_u32_e32 v3, vcc, 0, v3, vcc
	global_load_dwordx4 v[148:151], v[4:5], off
	global_load_dwordx4 v[152:155], v[2:3], off
	v_lshlrev_b64 v[2:3], 1, v[72:73]
	v_lshl_add_u64 v[4:5], s[4:5], 0, v[2:3]
	v_add_co_u32_e32 v6, vcc, s12, v4
	s_mov_b32 s4, 0x8000
	s_nop 0
	v_addc_co_u32_e32 v7, vcc, 0, v5, vcc
	v_add_co_u32_e32 v8, vcc, s4, v4
	s_mov_b32 s4, 0xa000
	s_nop 0
	v_addc_co_u32_e32 v9, vcc, 0, v5, vcc
	v_add_co_u32_e32 v4, vcc, s4, v4
	global_load_dwordx4 v[156:159], v[6:7], off
	global_load_dwordx4 v[160:163], v[8:9], off
	v_addc_co_u32_e32 v5, vcc, 0, v5, vcc
	global_load_dwordx4 v[164:167], v[4:5], off
	v_lshlrev_b32_e32 v4, 4, v192
	v_and_b32_e32 v5, 0xf0, v4
	s_movk_i32 s4, 0x60
	v_bitop3_b32 v204, v186, v5, s4 bitop3:0x36
	s_movk_i32 s4, 0x80
	v_bitop3_b32 v205, v186, v5, s4 bitop3:0x36
	s_movk_i32 s4, 0xa0
	v_bitop3_b32 v206, v186, v5, s4 bitop3:0x36
	s_movk_i32 s4, 0xe0
	v_bitop3_b32 v208, v186, v5, s4 bitop3:0x36
	s_movk_i32 s4, 0x100
	v_bitop3_b32 v209, v186, v5, s4 bitop3:0x36
	s_movk_i32 s4, 0x120
	s_movk_i32 s19, 0xf0
	v_bitop3_b32 v211, v186, v5, s4 bitop3:0x36
	s_movk_i32 s4, 0x140
	s_movk_i32 s16, 0x118
	s_cmp_lg_u32 0, -1
	v_bitop3_b32 v201, v186, v4, s19 bitop3:0x78
	v_bitop3_b32 v212, v186, v5, s4 bitop3:0x36
	s_movk_i32 s4, 0x160
	v_and_or_b32 v4, v26, s16, v28
	s_cselect_b32 s16, 0, 0
	v_and_b32_e32 v6, 15, v1
	s_waitcnt lgkmcnt(0)
	s_barrier
	s_load_dwordx4 s[12:15], s[22:23], 0xe8
	v_bitop3_b32 v202, v186, v5, 32 bitop3:0x36
	v_bitop3_b32 v203, v186, v5, 64 bitop3:0x36
	v_bitop3_b32 v207, v186, v5, s28 bitop3:0x36
	v_bitop3_b32 v213, v186, v5, s4 bitop3:0x36
	s_load_dwordx2 s[18:19], s[22:23], 0xa0
	s_load_dwordx2 s[20:21], s[22:23], 0xb0
	v_add3_u32 v214, v27, s16, v4
	v_lshl_add_u64 v[4:5], s[24:25], 0, v[70:71]
	v_lshlrev_b32_e32 v66, 4, v6
	s_add_u32 s6, s6, s27
	v_lshl_add_u64 v[4:5], v[4:5], 0, v[66:67]
	s_addc_u32 s7, s7, s26
	v_lshl_add_u64 v[4:5], s[8:9], 0, v[4:5]
	s_mov_b64 s[8:9], 0xa000
	v_lshl_add_u64 v[2:3], s[6:7], 0, v[2:3]
	s_mov_b64 s[6:7], 0x10000
	v_mov_b32_e32 v66, v67
	v_cvt_pk_bf16_f32 v142, v38, v39
	v_lshl_add_u64 v[188:189], v[4:5], 0, s[8:9]
	v_lshl_add_u64 v[190:191], v[2:3], 0, s[6:7]
	v_mov_b32_e32 v68, v67
	v_mov_b32_e32 v69, v67
	v_mov_b32_e32 v70, v67
	v_mov_b32_e32 v71, v67
	v_mov_b32_e32 v72, v67
	v_mov_b32_e32 v73, v67
	v_mov_b32_e32 v74, v67
	v_mov_b32_e32 v75, v67
	v_mov_b32_e32 v76, v67
	v_mov_b32_e32 v78, v67
	v_mov_b32_e32 v79, v67
	v_mov_b32_e32 v80, v67
	v_mov_b32_e32 v81, v67
	v_mov_b64_e32 v[50:51], v[66:67]
	v_mov_b64_e32 v[34:35], v[66:67]
	v_mov_b64_e32 v[18:19], v[66:67]
	v_mov_b64_e32 v[2:3], v[66:67]
	v_cvt_pk_bf16_f32 v132, v86, v87
	v_lshlrev_b32_e32 v200, 9, v192
	v_cmp_gt_u32_e64 s[4:5], 32, v187
	v_lshl_add_u32 v210, v192, 2, v185
	v_mov_b32_e32 v215, 0xf149f2ca
	s_movk_i32 s28, 0xbc00
	s_mov_b32 s34, -2
	s_movk_i32 s29, 0x84
	s_movk_i32 s30, 0x7ff
	s_mov_b32 s31, 0x42ddb3d8
	s_mov_b64 s[8:9], 0x4000
	s_mov_b64 s[22:23], 0x6000
	v_mov_b32_e32 v216, 0xfffff800
	v_mov_b32_e32 v217, 0x80
	v_mov_b64_e32 v[52:53], v[68:69]
	v_mov_b64_e32 v[54:55], v[70:71]
	v_mov_b64_e32 v[56:57], v[72:73]
	v_mov_b64_e32 v[58:59], v[74:75]
	v_mov_b64_e32 v[60:61], v[76:77]
	v_mov_b64_e32 v[62:63], v[78:79]
	v_mov_b64_e32 v[64:65], v[80:81]
	v_mov_b64_e32 v[36:37], v[68:69]
	v_mov_b64_e32 v[38:39], v[70:71]
	v_mov_b64_e32 v[40:41], v[72:73]
	v_mov_b64_e32 v[42:43], v[74:75]
	v_mov_b64_e32 v[44:45], v[76:77]
	v_mov_b64_e32 v[46:47], v[78:79]
	v_mov_b64_e32 v[48:49], v[80:81]
	v_mov_b64_e32 v[20:21], v[68:69]
	v_mov_b64_e32 v[22:23], v[70:71]
	v_mov_b64_e32 v[24:25], v[72:73]
	v_mov_b64_e32 v[26:27], v[74:75]
	v_mov_b64_e32 v[28:29], v[76:77]
	v_mov_b64_e32 v[30:31], v[78:79]
	v_mov_b64_e32 v[32:33], v[80:81]
	v_mov_b64_e32 v[4:5], v[68:69]
	v_mov_b64_e32 v[6:7], v[70:71]
	v_mov_b64_e32 v[8:9], v[72:73]
	v_mov_b64_e32 v[10:11], v[74:75]
	v_mov_b64_e32 v[12:13], v[76:77]
	v_mov_b64_e32 v[14:15], v[78:79]
	v_mov_b64_e32 v[16:17], v[80:81]
	v_mov_b32_e32 v218, 0
	s_waitcnt lgkmcnt(0)
	s_waitcnt vmcnt(0)
	s_lshr_b32 s56, s2, 1
	s_and_b32 s57, s56, 31
	s_lshl_b32 s57, s57, 7
	s_or_b32 s57, s57, s53
	s_lshr_b32 s58, s56, 5
	s_lshl_b32 s58, s58, 7
	s_and_b32 s59, s56, 15
	s_lshl_b32 s59, s59, 7
	s_or_b32 s59, s59, s53
	s_lshr_b32 s60, s56, 4
	s_lshl_b32 s60, s60, 7
	v_lshrrev_b32_e32 v253, 3, v0
	v_and_b32_e32 v254, 7, v0
	v_lshlrev_b32_e32 v254, 4, v254
	v_mul_u32_u24_e32 v244, 0x84, v253
	v_add_u32_e32 v244, v244, v254
	v_add_u32_e32 v244, 0x20800, v244
	v_and_b32_e32 v255, 15, v0
	v_mul_u32_u24_e32 v245, 0x210, v255
	v_lshrrev_b32_e32 v252, 4, v0
	v_lshl_add_u32 v245, v252, 2, v245
	v_add_u32_e32 v245, 0x20800, v245
	v_add_u32_e32 v246, s57, v253
	v_and_b32_e32 v247, 0x7ff, v246
	v_lshrrev_b32_e32 v246, 11, v246
	v_lshlrev_b32_e32 v246, 7, v246
	v_and_b32_e32 v251, 0x7f, v247
	v_or_b32_e32 v246, v246, v251
	v_lshrrev_b32_e32 v247, 7, v247
	v_lshl_or_b32 v246, v247, 8, v246
	v_lshlrev_b32_e32 v246, 11, v246
	v_add_u32_e32 v246, v246, v254
	v_add_u32_e32 v246, s58, v246
	v_add_u32_e32 v247, s59, v253
	v_lshlrev_b32_e32 v247, 11, v247
	v_add_u32_e32 v247, v247, v254
	v_add_u32_e32 v247, s60, v247
	v_lshlrev_b32_e32 v251, 2, v252
	v_lshlrev_b32_e32 v255, 2, v255
	v_add_u32_e32 v248, s58, v251
	v_lshlrev_b32_e32 v248, 14, v248
	v_add_u32_e32 v249, s57, v255
	v_lshl_add_u32 v248, v249, 2, v248
	v_add_u32_e32 v252, s60, v251
	v_lshlrev_b32_e32 v252, 13, v252
	v_add_u32_e32 v249, s59, v255
	v_lshl_add_u32 v252, v249, 2, v252
	v_add_u32_e32 v249, 0x4000, v248
	v_add_u32_e32 v250, 0x8000, v248
	v_add_u32_e32 v251, 0xc000, v248
	s_add_u32 s62, s18, 0x22000000
	s_addc_u32 s63, s19, 0
	s_add_i32 s37, s34, 2
	s_and_b32 s36, s37, 1
	s_cmpk_eq_i32 s34, 0x41
	s_cbranch_scc0 .LBB0_893

; DEV int ltid() { int t = threadIdx.x; asm volatile("" : "+v"(t)); return t; }
; DEV unsigned cvt_pk_bf16(float lo, float hi) { const f32x2 v = {lo, hi}; const bf16n2 r = __builtin_convertvector(v, bf16n2); return __builtin_bit_cast(unsigned, r); }
; DEV float bf2f(bf16_t v) { return __uint_as_float(((unsigned)v) << 16); }
; DEV int v_st(int k, int c) { const int kk = (k & ~0xC) | ((k & 4) << 1) | ((k & 8) >> 1); return ((kk >> 3) * 4 + (c >> 5)) * 512 + ((kk & 7) * 32 + (c & 31)) * 2; }
; DEV void fill_load(CParams& p, int wg, int slot, f32x4 (&ld)[4]) {
;   const FillDesc d = fill_decode(p, wg, slot); const int tid = ltid(), tx = tid & 15, ty = tid >> 4;
;   const float* sp = d.src + (long)(d.kh + 4 * ty) * d.ldsrc + d.n0 + 4 * tx;
; DEV void attn_unit(const bf16_t* __restrict__ Qb, const bf16_t* __restrict__ Kh, const bf16_t* __restrict__ Vh, const float* __restrict__ rp, bf16_t* __restrict__ Ob, CParams& fp, int fwg, int fbase, int fn) {
;     ...
; #pragma unroll
;     for (int dd = 0; dd < 2; ++dd) {
;       const int a0 = 16 * dd + 8 * hi;
;       const f32x4 c0 = *(const f32x4*)(rr + a0), c1 = *(const f32x4*)(rr + a0 + 4), s0 = *(const f32x4*)(rr + 32 + a0), s1 = *(const f32x4*)(rr + 32 + a0 + 4);
;       float cs[8] = {c0[0], c0[1], c0[2], c0[3], c1[0], c1[1], c1[2], c1[3]}, sn[8] = {s0[0], s0[1], s0[2], s0[3], s1[0], s1[1], s1[2], s1[3]};
;       const bf16x8 x1 = qr[8 + dd], x2 = qr[10 + dd]; bf16x8 y1, y2;
; #pragma unroll
;       for (int j = 0; j < 8; j += 2) {
;         const float a1 = bf2f((bf16_t)x1[j]), a2 = bf2f((bf16_t)x2[j]), b1 = bf2f((bf16_t)x1[j + 1]), b2 = bf2f((bf16_t)x2[j + 1]);
;         const unsigned u1 = cvt_pk_bf16(a1 * cs[j] - a2 * sn[j], b1 * cs[j + 1] - b2 * sn[j + 1]);
;         const unsigned u2 = cvt_pk_bf16(a1 * sn[j] + a2 * cs[j], b1 * sn[j + 1] + b2 * cs[j + 1]);
;         y1[j] = (short)(u1 & 0xffff); y1[j + 1] = (short)(u1 >> 16); y2[j] = (short)(u2 & 0xffff); y2[j + 1] = (short)(u2 >> 16);
;       }
;       qr[8 + dd] = y1; qr[10 + dd] = y2;
;     }
;   }
;   const int sr = tid >> 4, sc = (tid & 15) * 8, vst0 = v_st(sr, sc), vst1 = v_st(32 + sr, sc);
;   int kst[3];
; #pragma unroll
;   for (int i = 0; i < 3; ++i) { const int id = tid + 512 * i, row = id / 24, ch = id % 24; kst[i] = KSWZ2(row, ch * 16); }
.LBB0_1097:
	s_waitcnt vmcnt(11)
	v_and_b32_e32 v81, 0xffff0000, v58
	v_lshlrev_b32_e32 v80, 16, v58
	s_waitcnt vmcnt(9)
	v_and_b32_e32 v83, 0xffff0000, v50
	v_lshlrev_b32_e32 v82, 16, v50
	s_waitcnt vmcnt(4)
	v_pk_mul_f32 v[84:85], v[66:67], v[82:83]
	v_pk_mul_f32 v[66:67], v[66:67], v[80:81]
	v_pk_fma_f32 v[84:85], v[62:63], v[80:81], v[84:85] neg_lo:[0,0,1] neg_hi:[0,0,1]
	v_pk_fma_f32 v[62:63], v[62:63], v[82:83], v[66:67]
	v_lshlrev_b32_e32 v58, 16, v51
	v_cvt_pk_bf16_f32 v136, v62, v63
	v_and_b32_e32 v63, 0xffff0000, v59
	v_lshlrev_b32_e32 v62, 16, v59
	v_and_b32_e32 v59, 0xffff0000, v51
	v_pk_mul_f32 v[50:51], v[68:69], v[58:59]
	s_mov_b32 s21, 0x2aaaaaab
	v_pk_fma_f32 v[50:51], v[64:65], v[62:63], v[50:51] neg_lo:[0,0,1] neg_hi:[0,0,1]
	s_lshl_b32 s23, s17, 7
	v_cvt_pk_bf16_f32 v133, v50, v51
	v_pk_mul_f32 v[50:51], v[68:69], v[62:63]
	s_lshl_b32 s17, s17, s22
	v_pk_fma_f32 v[50:51], v[64:65], v[58:59], v[50:51]
	v_and_b32_e32 v59, 0xffff0000, v52
	v_lshlrev_b32_e32 v58, 16, v52
	v_cvt_pk_bf16_f32 v137, v50, v51
	v_and_b32_e32 v51, 0xffff0000, v60
	v_lshlrev_b32_e32 v50, 16, v60
	v_pk_mul_f32 v[62:63], v[54:55], v[58:59]
	s_and_b32 s17, s17, 0x780
	v_pk_fma_f32 v[62:63], v[46:47], v[50:51], v[62:63] neg_lo:[0,0,1] neg_hi:[0,0,1]
	v_pk_mul_f32 v[50:51], v[54:55], v[50:51]
	s_and_b32 s18, s18, s23
	v_pk_fma_f32 v[46:47], v[46:47], v[58:59], v[50:51]
	v_and_b32_e32 v51, 0xffff0000, v53
	v_lshlrev_b32_e32 v50, 16, v53
	v_cvt_pk_bf16_f32 v138, v46, v47
	v_and_b32_e32 v47, 0xffff0000, v61
	v_lshlrev_b32_e32 v46, 16, v61
	v_pk_mul_f32 v[52:53], v[56:57], v[50:51]
	s_or_b32 s18, s18, s53
	v_pk_fma_f32 v[52:53], v[48:49], v[46:47], v[52:53] neg_lo:[0,0,1] neg_hi:[0,0,1]
	v_pk_mul_f32 v[46:47], v[56:57], v[46:47]
	s_mov_b32 s19, 0
	v_pk_fma_f32 v[46:47], v[48:49], v[50:51], v[46:47]
	v_and_b32_e32 v49, 0xffff0000, v22
	v_cvt_pk_bf16_f32 v139, v46, v47
	v_and_b32_e32 v47, 0xffff0000, v30
	v_lshlrev_b32_e32 v46, 16, v30
	v_lshlrev_b32_e32 v48, 16, v22
	s_waitcnt vmcnt(0)
	v_pk_mul_f32 v[50:51], v[42:43], v[48:49]
	v_pk_mul_f32 v[42:43], v[42:43], v[46:47]
	v_pk_fma_f32 v[50:51], v[38:39], v[46:47], v[50:51] neg_lo:[0,0,1] neg_hi:[0,0,1]
	v_pk_fma_f32 v[38:39], v[38:39], v[48:49], v[42:43]
	v_lshlrev_b32_e32 v30, 16, v23
	v_cvt_pk_bf16_f32 v144, v38, v39
	v_and_b32_e32 v39, 0xffff0000, v31
	v_lshlrev_b32_e32 v38, 16, v31
	v_and_b32_e32 v31, 0xffff0000, v23
	v_pk_mul_f32 v[22:23], v[44:45], v[30:31]
	s_lshl_b32 s18, s18, 2
	v_pk_fma_f32 v[22:23], v[40:41], v[38:39], v[22:23] neg_lo:[0,0,1] neg_hi:[0,0,1]
	v_mov_b32_e32 v67, 0
	v_cvt_pk_bf16_f32 v141, v22, v23
	v_pk_mul_f32 v[22:23], v[44:45], v[38:39]
	v_mov_b32_e32 v253, v67
	v_pk_fma_f32 v[22:23], v[40:41], v[30:31], v[22:23]
	v_and_b32_e32 v31, 0xffff0000, v24
	v_lshlrev_b32_e32 v30, 16, v24
	v_cvt_pk_bf16_f32 v145, v22, v23
	v_and_b32_e32 v23, 0xffff0000, v32
	v_lshlrev_b32_e32 v22, 16, v32
	v_pk_mul_f32 v[38:39], v[34:35], v[30:31]
	v_and_b32_e32 v77, 0x3fffffc0, v1
	v_pk_fma_f32 v[38:39], v[26:27], v[22:23], v[38:39] neg_lo:[0,0,1] neg_hi:[0,0,1]
	v_pk_mul_f32 v[22:23], v[34:35], v[22:23]
	v_lshl_add_u32 v185, v77, 2, s77
	v_pk_fma_f32 v[22:23], v[26:27], v[30:31], v[22:23]
	v_and_b32_e32 v27, 0xffff0000, v25
	v_lshlrev_b32_e32 v26, 16, v25
	v_cvt_pk_bf16_f32 v146, v22, v23
	v_and_b32_e32 v23, 0xffff0000, v33
	v_lshlrev_b32_e32 v22, 16, v33
	v_pk_mul_f32 v[24:25], v[36:37], v[26:27]
	v_cvt_pk_bf16_f32 v134, v62, v63
	v_pk_fma_f32 v[24:25], v[28:29], v[22:23], v[24:25] neg_lo:[0,0,1] neg_hi:[0,0,1]
	v_pk_mul_f32 v[22:23], v[36:37], v[22:23]
	v_cvt_pk_bf16_f32 v143, v24, v25
	v_pk_fma_f32 v[22:23], v[28:29], v[26:27], v[22:23]
	v_and_b32_e32 v25, 3, v74
	v_cvt_pk_bf16_f32 v147, v22, v23
	v_and_b32_e32 v22, 0xfffff0, v74
	v_lshlrev_b32_e32 v23, 1, v74
	v_and_or_b32 v22, v23, 8, v22
	v_lshrrev_b32_e32 v23, 1, v74
	v_and_or_b32 v23, v23, 4, v25
	v_and_b32_e32 v25, 0xfffff0, v76
	v_lshlrev_b32_e32 v26, 1, v76
	v_and_or_b32 v25, v26, 8, v25
	v_lshrrev_b32_e32 v22, 1, v22
	v_lshrrev_b32_e32 v24, 5, v78
	v_lshrrev_b32_e32 v25, 1, v25
	v_or_b32_e32 v22, v22, v24
	v_or_b32_e32 v24, v25, v24
	v_mul_hi_i32 v25, v1, s21
	v_lshrrev_b32_e32 v26, 31, v25
	v_ashrrev_i32_e32 v25, 2, v25
	v_add_u32_e32 v25, v25, v26
	v_mul_lo_u32 v26, v25, 24
	v_sub_u32_e32 v26, v1, v26
	v_lshlrev_b32_e32 v27, 9, v25
	v_bitop3_b32 v25, v25, v26, 15 bitop3:0x6c
	v_lshl_add_u32 v195, v25, 4, v27
	v_add_u32_e32 v25, 0x200, v1
	v_mul_hi_i32 v26, v25, s21
	v_lshrrev_b32_e32 v27, 31, v26
	v_ashrrev_i32_e32 v26, 2, v26
	v_add_u32_e32 v26, v26, v27
	v_mul_lo_u32 v27, v26, 24
	v_sub_u32_e32 v25, v25, v27
	v_lshlrev_b32_e32 v27, 9, v26
	v_bitop3_b32 v25, v26, v25, 15 bitop3:0x6c
	v_lshl_add_u32 v196, v25, 4, v27
	v_add_u32_e32 v25, 0x400, v1
	v_mul_hi_i32 v26, v25, s21
	v_lshrrev_b32_e32 v27, 31, v26
	v_ashrrev_i32_e32 v26, 2, v26
	v_add_u32_e32 v26, v26, v27
	v_mul_lo_u32 v27, v26, 24
	v_sub_u32_e32 v25, v25, v27
	v_lshlrev_b32_e32 v27, 9, v26
	v_bitop3_b32 v25, v26, v25, 15 bitop3:0x6c
	v_lshlrev_b32_e32 v22, 9, v22
	v_lshlrev_b32_e32 v23, 6, v23
	v_lshl_add_u32 v197, v25, 4, v27
	v_and_b32_e32 v25, 48, v252
	v_lshlrev_b32_e32 v24, 9, v24
	v_or3_b32 v198, v22, v23, v25
	v_lshlrev_b32_e32 v22, 4, v187
	v_or3_b32 v199, v24, v23, v25
	v_and_b32_e32 v27, 0xc0, v22
	v_lshlrev_b32_e32 v22, 1, v187
	v_mov_b32_e32 v24, v0
	v_and_b32_e32 v28, 32, v22
	v_lshlrev_b32_e32 v26, 3, v187
	v_ashrrev_i32_e32 v22, 2, v24
	v_and_b32_e32 v22, -4, v22
	v_add_u32_e32 v22, s17, v22
	v_mad_i64_i32 v[22:23], s[22:23], s20, v22, 0
	v_lshl_add_u64 v[22:23], v[22:23], 2, s[14:15]
	v_lshlrev_b32_e32 v24, 4, v24
	v_lshl_add_u64 v[22:23], v[22:23], 0, s[18:19]
; DEV int v_rd_base(int lane) { return ((lane & 3) << 3) | (((lane >> 2) & 3) << 6) | (((lane >> 4) & 1) << 5) | (((lane >> 5) & 1) << 8); }
; #define SLOAD(k0) do { vs0 = *reinterpret_cast<const bf16x8*>(Vh + (long)((k0) + sr) * DV + sc); vs1 = *reinterpret_cast<const bf16x8*>(Vh + (long)((k0) + 32 + sr) * DV + sc); \
;     const bf16_t* kp_ = Kh + (long)(k0) * QK + tid * 8; ks0 = *reinterpret_cast<const bf16x8*>(kp_); ks1 = *reinterpret_cast<const bf16x8*>(kp_ + 4096); ks2 = *reinterpret_cast<const bf16x8*>(kp_ + 8192); } while (0)
; #define SWRITE(b) do { *(bf16x8*)(V_lds + (b) * SHM_V + vst0) = vs0; *(bf16x8*)(V_lds + (b) * SHM_V + vst1) = vs1; \
;     *(bf16x8*)(K_lds + (b) * SHM_K + kst[0]) = ks0; *(bf16x8*)(K_lds + (b) * SHM_K + kst[1]) = ks1; *(bf16x8*)(K_lds + (b) * SHM_K + kst[2]) = ks2; } while (0)
; #define SWAIT() asm volatile("s_waitcnt vmcnt(0)" ::: "memory")
; DEV void attn_unit(const bf16_t* __restrict__ Qb, const bf16_t* __restrict__ Kh, const bf16_t* __restrict__ Vh, const float* __restrict__ rp, bf16_t* __restrict__ Ob, CParams& fp, int fwg, int fbase, int fn) {
;     ...
;   const int vb0 = (int)(uintptr_t)V_lds + v_rd_base(lane);
;     ...
;   f32x16 p0, p1; float mn, al; bf16x8 pa0, pa1, pa2, pa3; constexpr int NTL = KEYS / KVBLK;
;   f32x4 fld[4];
;   if (fn > 0) fill_load(fp, fwg, fbase, fld);
;   SWRITE(0); SLOAD(KVBLK); __syncthreads();
; #pragma unroll 1
;   for (int j = 0; j < NTL; ++j) {
;     const int cb = j & 1;
;     if (j + 1 < NTL) { if (j >= 2 && j < fn) asm volatile("s_waitcnt vmcnt(5)" ::: "memory"); else SWAIT(); SWRITE(cb ^ 1); }
	v_and_b32_e32 v66, 0xf0, v24
	v_lshl_add_u64 v[22:23], v[22:23], 0, v[66:67]
	s_lshl_b32 s18, s20, 2
	v_lshl_add_u64 v[24:25], v[22:23], 0, s[18:19]
	global_load_dwordx4 v[168:171], v[22:23], off
	global_load_dwordx4 v[172:175], v[24:25], off
	v_lshl_add_u64 v[22:23], v[24:25], 0, s[18:19]
	v_lshl_add_u64 v[24:25], v[22:23], 0, s[18:19]
	global_load_dwordx4 v[176:179], v[22:23], off
	global_load_dwordx4 v[180:183], v[24:25], off
	v_add_u32_e32 v22, 0, v198
	ds_write_b128 v22, v[6:9]
	v_add_u32_e32 v6, 0, v199
	ds_write_b128 v6, v[2:5]
	v_add_u32_e32 v2, 0, v195
	ds_write_b128 v2, v[10:13] offset:32768
	v_add_u32_e32 v2, 0, v196
	ds_write_b128 v2, v[14:17] offset:32768
	v_add_u32_e32 v2, 0, v197
	ds_write_b128 v2, v[18:21] offset:32768
	v_lshlrev_b64 v[2:3], 8, v[74:75]
	v_lshl_add_u64 v[2:3], s[12:13], 0, v[2:3]
	v_lshl_add_u64 v[2:3], v[2:3], 0, v[252:253]
	s_movk_i32 s12, 0x4000
	v_add_co_u32_e32 v4, vcc, s12, v2
	s_movk_i32 s12, 0x6000
	s_nop 0
	v_addc_co_u32_e32 v5, vcc, 0, v3, vcc
	v_add_co_u32_e32 v2, vcc, s12, v2
	s_movk_i32 s17, 0xf0
	s_nop 0
	v_addc_co_u32_e32 v3, vcc, 0, v3, vcc
	global_load_dwordx4 v[148:151], v[4:5], off
	global_load_dwordx4 v[152:155], v[2:3], off
	v_lshlrev_b64 v[2:3], 1, v[72:73]
	v_lshl_add_u64 v[4:5], s[4:5], 0, v[2:3]
	v_add_co_u32_e32 v6, vcc, s12, v4
	s_mov_b32 s4, 0x8000
	s_nop 0
	v_addc_co_u32_e32 v7, vcc, 0, v5, vcc
	v_add_co_u32_e32 v8, vcc, s4, v4
	s_mov_b32 s4, 0xa000
	s_nop 0
	v_addc_co_u32_e32 v9, vcc, 0, v5, vcc
	v_add_co_u32_e32 v4, vcc, s4, v4
	global_load_dwordx4 v[156:159], v[6:7], off
	global_load_dwordx4 v[160:163], v[8:9], off
	v_addc_co_u32_e32 v5, vcc, 0, v5, vcc
	global_load_dwordx4 v[164:167], v[4:5], off
	v_lshlrev_b32_e32 v4, 4, v192
	v_and_b32_e32 v5, 0xf0, v4
	s_movk_i32 s4, 0x60
	v_bitop3_b32 v204, v186, v5, s4 bitop3:0x36
	s_movk_i32 s4, 0x80
	v_bitop3_b32 v205, v186, v5, s4 bitop3:0x36
	s_movk_i32 s4, 0xa0
	v_bitop3_b32 v206, v186, v5, s4 bitop3:0x36
	s_movk_i32 s4, 0xe0
	v_bitop3_b32 v208, v186, v5, s4 bitop3:0x36
	s_movk_i32 s4, 0x100
	v_bitop3_b32 v201, v186, v4, s17 bitop3:0x78
	v_bitop3_b32 v209, v186, v5, s4 bitop3:0x36
	s_movk_i32 s4, 0x120
	s_movk_i32 s17, 0x118
	s_cmp_lg_u32 0, -1
	v_bitop3_b32 v211, v186, v5, s4 bitop3:0x36
	s_movk_i32 s4, 0x140
	v_and_or_b32 v4, v26, s17, v28
	s_cselect_b32 s17, 0, 0
	s_movk_i32 s21, 0xc0
	v_bitop3_b32 v212, v186, v5, s4 bitop3:0x36
	s_movk_i32 s4, 0x160
	v_add3_u32 v214, v27, s17, v4
	s_add_i32 s17, s2, 0x8300
	v_mov_b32_e32 v4, 0x110000
	v_and_b32_e32 v6, 15, v1
	s_waitcnt lgkmcnt(0)
	s_barrier
	s_load_dwordx4 s[12:15], s[24:25], 0xe8
	v_bitop3_b32 v202, v186, v5, 32 bitop3:0x36
	v_bitop3_b32 v203, v186, v5, 64 bitop3:0x36
	v_bitop3_b32 v207, v186, v5, s21 bitop3:0x36
	v_bitop3_b32 v213, v186, v5, s4 bitop3:0x36
	s_load_dwordx2 s[20:21], s[24:25], 0xa0
	s_load_dwordx2 s[22:23], s[24:25], 0xb0
	v_mad_i64_i32 v[4:5], s[24:25], s16, v4, v[70:71]
	v_lshlrev_b32_e32 v66, 4, v6
	s_add_u32 s6, s6, s27
	v_lshl_add_u64 v[4:5], v[4:5], 0, v[66:67]
	s_addc_u32 s7, s7, s26
	v_lshl_add_u64 v[4:5], s[8:9], 0, v[4:5]
	s_mov_b64 s[8:9], 0xa000
	v_lshl_add_u64 v[2:3], s[6:7], 0, v[2:3]
	s_mov_b64 s[6:7], 0x10000
	v_mov_b32_e32 v66, v67
	v_cvt_pk_bf16_f32 v135, v52, v53
	v_cvt_pk_bf16_f32 v140, v50, v51
	v_cvt_pk_bf16_f32 v142, v38, v39
	v_lshl_add_u64 v[188:189], v[4:5], 0, s[8:9]
	v_lshl_add_u64 v[190:191], v[2:3], 0, s[6:7]
	v_mov_b32_e32 v68, v67
	v_mov_b32_e32 v69, v67
	v_mov_b32_e32 v70, v67
	v_mov_b32_e32 v71, v67
	v_mov_b32_e32 v72, v67
	v_mov_b32_e32 v73, v67
	v_mov_b32_e32 v74, v67
	v_mov_b32_e32 v75, v67
	v_mov_b32_e32 v76, v67
	v_mov_b32_e32 v77, v67
	v_mov_b32_e32 v78, v67
	v_mov_b32_e32 v79, v67
	v_mov_b32_e32 v80, v67
	v_mov_b32_e32 v81, v67
	v_mov_b64_e32 v[50:51], v[66:67]
	v_mov_b64_e32 v[34:35], v[66:67]
	v_mov_b64_e32 v[18:19], v[66:67]
	v_mov_b64_e32 v[2:3], v[66:67]
	v_cvt_pk_bf16_f32 v132, v84, v85
	v_lshlrev_b32_e32 v200, 9, v192
	v_cmp_gt_u32_e64 s[4:5], 32, v187
	v_lshl_add_u32 v210, v192, 2, v185
	v_mov_b32_e32 v215, 0xf149f2ca
	s_mov_b32 s35, -2
	s_movk_i32 s30, 0x84
	s_movk_i32 s31, 0x7ff
	s_mov_b32 s34, 0x42ddb3d8
	s_mov_b64 s[8:9], 0x4000
	s_mov_b64 s[24:25], 0x6000
	v_mov_b32_e32 v216, 0xfffff800
	v_mov_b32_e32 v217, 0x80
	v_mov_b64_e32 v[52:53], v[68:69]
	v_mov_b64_e32 v[54:55], v[70:71]
	v_mov_b64_e32 v[56:57], v[72:73]
	v_mov_b64_e32 v[58:59], v[74:75]
	v_mov_b64_e32 v[60:61], v[76:77]
	v_mov_b64_e32 v[62:63], v[78:79]
	v_mov_b64_e32 v[64:65], v[80:81]
	v_mov_b64_e32 v[36:37], v[68:69]
	v_mov_b64_e32 v[38:39], v[70:71]
	v_mov_b64_e32 v[40:41], v[72:73]
	v_mov_b64_e32 v[42:43], v[74:75]
	v_mov_b64_e32 v[44:45], v[76:77]
	v_mov_b64_e32 v[46:47], v[78:79]
	v_mov_b64_e32 v[48:49], v[80:81]
	v_mov_b64_e32 v[20:21], v[68:69]
	v_mov_b64_e32 v[22:23], v[70:71]
	v_mov_b64_e32 v[24:25], v[72:73]
	v_mov_b64_e32 v[26:27], v[74:75]
	v_mov_b64_e32 v[28:29], v[76:77]
	v_mov_b64_e32 v[30:31], v[78:79]
	v_mov_b64_e32 v[32:33], v[80:81]
	v_mov_b64_e32 v[4:5], v[68:69]
	v_mov_b64_e32 v[6:7], v[70:71]
	v_mov_b64_e32 v[8:9], v[72:73]
	v_mov_b64_e32 v[10:11], v[74:75]
	v_mov_b64_e32 v[12:13], v[76:77]
	v_mov_b64_e32 v[14:15], v[78:79]
	v_mov_b64_e32 v[16:17], v[80:81]
	v_mov_b32_e32 v218, 0
	s_waitcnt lgkmcnt(0)
	s_waitcnt vmcnt(0)
	s_lshr_b32 s56, s2, 1
	s_and_b32 s57, s56, 31
	s_lshl_b32 s57, s57, 7
	s_or_b32 s57, s57, s53
	s_lshr_b32 s58, s56, 5
	s_lshl_b32 s58, s58, 7
	s_and_b32 s59, s56, 15
	s_lshl_b32 s59, s59, 7
	s_or_b32 s59, s59, s53
	s_lshr_b32 s60, s56, 4
	s_lshl_b32 s60, s60, 7
	v_lshrrev_b32_e32 v253, 3, v0
	v_and_b32_e32 v254, 7, v0
	v_lshlrev_b32_e32 v254, 4, v254
	v_mul_u32_u24_e32 v244, 0x84, v253
	v_add_u32_e32 v244, v244, v254
	v_add_u32_e32 v244, 0x20800, v244
	v_and_b32_e32 v255, 15, v0
	v_mul_u32_u24_e32 v245, 0x210, v255
	v_lshrrev_b32_e32 v252, 4, v0
	v_lshl_add_u32 v245, v252, 2, v245
	v_add_u32_e32 v245, 0x20800, v245
	v_add_u32_e32 v246, s57, v253
	v_and_b32_e32 v247, 0x7ff, v246
	v_lshrrev_b32_e32 v246, 11, v246
	v_lshlrev_b32_e32 v246, 7, v246
	v_and_b32_e32 v251, 0x7f, v247
	v_or_b32_e32 v246, v246, v251
	v_lshrrev_b32_e32 v247, 7, v247
	v_lshl_or_b32 v246, v247, 8, v246
	v_lshlrev_b32_e32 v246, 11, v246
	v_add_u32_e32 v246, v246, v254
	v_add_u32_e32 v246, s58, v246
	v_add_u32_e32 v247, s59, v253
	v_lshlrev_b32_e32 v247, 11, v247
	v_add_u32_e32 v247, v247, v254
	v_add_u32_e32 v247, s60, v247
	v_lshlrev_b32_e32 v251, 2, v252
	v_lshlrev_b32_e32 v255, 2, v255
	v_add_u32_e32 v248, s58, v251
	v_lshlrev_b32_e32 v248, 14, v248
	v_add_u32_e32 v249, s57, v255
	v_lshl_add_u32 v248, v249, 2, v248
	v_add_u32_e32 v252, s60, v251
	v_lshlrev_b32_e32 v252, 13, v252
	v_add_u32_e32 v249, s59, v255
	v_lshl_add_u32 v252, v249, 2, v252
	v_mov_b32_e32 v248, v252
	v_add_u32_e32 v249, 0x2000, v252
	v_add_u32_e32 v250, 0x4000, v252
	v_add_u32_e32 v251, 0x6000, v252
	s_add_u32 s62, s22, 0x1800000
	s_addc_u32 s63, s23, 0
	s_add_i32 s38, s35, 2
	s_and_b32 s37, s38, 1
	s_cmpk_eq_i32 s35, 0x41
	s_cbranch_scc0 .LBB0_1100
